# DSA tile loop: 16 selection-bit tests rewritten as v_bfe_i32 + v_bfi_b32 (bit-exact -inf masking, one VALU op fewer per score, no SGPR round trip)
# baseline (speedup 1.0000x reference)
.LBB0_626:
	s_and_b32 s4, s9, 0x8000
	s_add_i32 s20, s4, 0
	v_add_u32_e32 v219, s20, v194
	v_mov_b32_e32 v237, v195
	s_nop 0
	v_xad_u32 v130, v237, v180, v219
	ds_read_b128 v[130:133], v130 offset:16384
	v_xad_u32 v134, v237, v196, v219
	ds_read_b128 v[220:223], v134 offset:16384
	v_xad_u32 v224, v237, v200, v219
	v_xad_u32 v228, v237, v201, v219
	ds_read_b128 v[224:227], v224 offset:16384
	ds_read_b128 v[228:231], v228 offset:16384
	s_waitcnt lgkmcnt(0)
	v_mfma_f32_32x32x16_bf16 v[130:145], v[130:133], v[146:149], 0
	v_mfma_f32_32x32x16_bf16 v[130:145], v[220:223], v[150:153], v[130:145]
	v_mfma_f32_32x32x16_bf16 v[130:145], v[224:227], v[154:157], v[130:145]
	v_xad_u32 v220, v237, v202, v219
	v_xad_u32 v224, v237, v203, v219
	ds_read_b128 v[220:223], v220 offset:16384
	ds_read_b128 v[224:227], v224 offset:16384
	v_mfma_f32_32x32x16_bf16 v[130:145], v[228:231], v[158:161], v[130:145]
	s_waitcnt lgkmcnt(0)
	v_mfma_f32_32x32x16_bf16 v[130:145], v[220:223], v[162:165], v[130:145]
	v_xad_u32 v220, v237, v204, v219
	v_xad_u32 v228, v237, v205, v219
	ds_read_b128 v[220:223], v220 offset:16384
	ds_read_b128 v[228:231], v228 offset:16384
	v_mfma_f32_32x32x16_bf16 v[130:145], v[224:227], v[166:169], v[130:145]
	s_waitcnt lgkmcnt(0)
	v_mfma_f32_32x32x16_bf16 v[130:145], v[220:223], v[170:173], v[130:145]
	v_xad_u32 v220, v237, v206, v219
	v_xad_u32 v224, v237, v207, v219
	ds_read_b128 v[220:223], v220 offset:16384
	ds_read_b128 v[224:227], v224 offset:16384
	ds_read_b128 v[232:235], v192
	ds_read_b128 v[238:241], v192 offset:1024
	v_mfma_f32_32x32x16_bf16 v[130:145], v[228:231], v[174:177], v[130:145]
	s_waitcnt lgkmcnt(0)
	v_mfma_f32_32x32x16_bf16 v[130:145], v[220:223], v[232:235], v[130:145]
	v_xad_u32 v220, v237, v208, v219
	v_xad_u32 v228, v237, v209, v219
	ds_read_b128 v[220:223], v220 offset:16384
	ds_read_b128 v[228:231], v228 offset:16384
	ds_read_b128 v[232:235], v192 offset:2048
	ds_read_b128 v[242:245], v192 offset:3072
	v_mfma_f32_32x32x16_bf16 v[130:145], v[224:227], v[238:241], v[130:145]
	s_waitcnt lgkmcnt(0)
	v_mfma_f32_32x32x16_bf16 v[130:145], v[220:223], v[232:235], v[130:145]
	v_xad_u32 v220, v237, v210, v219
	v_xad_u32 v224, v237, v211, v219
	ds_read_b128 v[220:223], v220 offset:16384
	ds_read_b128 v[224:227], v224 offset:16384
	ds_read_b128 v[232:235], v192 offset:4096
	ds_read_b128 v[238:241], v192 offset:5120
	v_mfma_f32_32x32x16_bf16 v[130:145], v[228:231], v[242:245], v[130:145]
	s_waitcnt lgkmcnt(0)
	v_mfma_f32_32x32x16_bf16 v[130:145], v[220:223], v[232:235], v[130:145]
	v_xad_u32 v220, v237, v212, v219
	v_xad_u32 v219, v237, v213, v219
	ds_read_b128 v[220:223], v220 offset:16384
	ds_read_b128 v[228:231], v219 offset:16384
	ds_read_b128 v[232:235], v192 offset:6144
	ds_read_b128 v[242:245], v192 offset:7168
	v_mfma_f32_32x32x16_bf16 v[130:145], v[224:227], v[238:241], v[130:145]
	s_waitcnt lgkmcnt(0)
	v_mfma_f32_32x32x16_bf16 v[130:145], v[220:223], v[232:235], v[130:145]
	v_mfma_f32_32x32x16_bf16 v[130:145], v[228:231], v[242:245], v[130:145]
	v_cvt_f32_i32_e32 v234, v215
	v_lshrrev_b32_e32 v218, v197, v218
	s_nop 9
	v_mul_f32_e32 v130, 0x3cb8aa3b, v130
	v_bfe_i32 v219, v218, 0, 1
	v_fma_f32 v130, v198, |v234|, v130
	v_bfi_b32 v219, v219, v130, v216
	v_mul_f32_e32 v131, 0x3cb8aa3b, v131
	v_mul_f32_e32 v132, 0x3cb8aa3b, v132

	v_add_f32_e32 v130, -1.0, v234
	v_fma_f32 v130, v198, |v130|, v131
	v_bfe_i32 v131, v218, 1, 1
	v_bfi_b32 v220, v131, v130, v216
	v_add_f32_e32 v131, -2.0, v234
	v_fma_f32 v131, v198, |v131|, v132
	v_bfe_i32 v132, v218, 2, 1

	v_bfi_b32 v221, v132, v131, v216
	v_mul_f32_e32 v132, 0x3cb8aa3b, v133
	v_max3_f32 v130, v219, s8, v220

	v_add_f32_e32 v131, 0xc0400000, v234
	v_fma_f32 v131, v198, |v131|, v132
	v_bfe_i32 v132, v218, 3, 1
	v_bfi_b32 v222, v132, v131, v216
	v_mul_f32_e32 v132, 0x3cb8aa3b, v134
	v_mov_b32_e32 v235, 1.0

	v_add_f32_e32 v131, 0xc1000000, v234
	v_fma_f32 v131, v198, |v131|, v132
	v_bfe_i32 v132, v218, 8, 1
	v_bfi_b32 v223, v132, v131, v216
	v_mul_f32_e32 v132, 0x3cb8aa3b, v135
	v_max3_f32 v130, v130, v221, v222

	v_add_f32_e32 v131, 0xc1100000, v234
	v_fma_f32 v131, v198, |v131|, v132
	v_bfe_i32 v132, v218, 9, 1
	v_bfi_b32 v224, v132, v131, v216
	v_mul_f32_e32 v132, 0x3cb8aa3b, v136


	v_add_f32_e32 v131, 0xc1200000, v234
	v_fma_f32 v131, v198, |v131|, v132
	v_bfe_i32 v132, v218, 10, 1
	v_bfi_b32 v225, v132, v131, v216
	v_mul_f32_e32 v132, 0x3cb8aa3b, v137
	v_max3_f32 v130, v130, v223, v224

	v_add_f32_e32 v131, 0xc1300000, v234
	v_fma_f32 v131, v198, |v131|, v132
	v_bfe_i32 v132, v218, 11, 1
	v_bfi_b32 v226, v132, v131, v216
	v_mul_f32_e32 v132, 0x3cb8aa3b, v138


	v_add_f32_e32 v131, 0xc1800000, v234
	v_fma_f32 v131, v198, |v131|, v132
	v_bfe_i32 v132, v218, 16, 1
	v_bfi_b32 v227, v132, v131, v216
	v_mul_f32_e32 v132, 0x3cb8aa3b, v139
	v_max3_f32 v130, v130, v225, v226

	v_add_f32_e32 v131, 0xc1880000, v234
	v_fma_f32 v131, v198, |v131|, v132
	v_bfe_i32 v132, v218, 17, 1
	v_bfi_b32 v228, v132, v131, v216
	v_mul_f32_e32 v132, 0x3cb8aa3b, v140


	v_add_f32_e32 v131, 0xc1900000, v234
	v_fma_f32 v131, v198, |v131|, v132
	v_bfe_i32 v132, v218, 18, 1
	v_bfi_b32 v229, v132, v131, v216
	v_mul_f32_e32 v132, 0x3cb8aa3b, v141
	v_max3_f32 v130, v130, v227, v228

	v_add_f32_e32 v131, 0xc1980000, v234
	v_fma_f32 v131, v198, |v131|, v132
	v_bfe_i32 v132, v218, 19, 1
	v_bfi_b32 v230, v132, v131, v216
	v_mul_f32_e32 v132, 0x3cb8aa3b, v142


	v_add_f32_e32 v131, 0xc1c00000, v234
	v_fma_f32 v131, v198, |v131|, v132
	v_bfe_i32 v132, v218, 24, 1
	v_bfi_b32 v231, v132, v131, v216
	v_mul_f32_e32 v132, 0x3cb8aa3b, v143
	v_max3_f32 v130, v130, v229, v230

	v_add_f32_e32 v131, 0xc1c80000, v234
	v_fma_f32 v131, v198, |v131|, v132
	v_bfe_i32 v132, v218, 25, 1
	v_bfi_b32 v232, v132, v131, v216
	v_mul_f32_e32 v132, 0x3cb8aa3b, v144


	v_add_f32_e32 v131, 0xc1d00000, v234
	v_fma_f32 v131, v198, |v131|, v132
	v_bfe_i32 v132, v218, 26, 1
	v_bfi_b32 v233, v132, v131, v216
	v_mul_f32_e32 v132, 0x3cb8aa3b, v145
	v_max3_f32 v130, v130, v231, v232

	v_add_f32_e32 v131, 0xc1d80000, v234
	v_fma_f32 v131, v198, |v131|, v132
	v_bfe_i32 v132, v218, 27, 1
	v_bfi_b32 v234, v132, v131, v216


	v_max3_f32 v130, v130, v233, v234
	v_mov_b32_e32 v131, v130
	s_nop 1
	v_permlane32_swap_b32_e32 v130, v131
	v_max_f32_e32 v131, v131, v131
	v_max_f32_e32 v130, v130, v130
	v_max_f32_e32 v130, v130, v131
	v_sub_f32_e32 v131, v130, v236
	v_cmp_ge_f32_e64 s[4:5], s18, v131
	s_cmp_eq_u64 s[4:5], exec
	s_cbranch_scc1 .LBB0_630
	v_max_f32_e32 v130, v130, v130
	v_max_f32_e32 v131, v236, v236
	v_max_f32_e32 v218, v131, v130
	v_sub_f32_e32 v130, v236, v218
	v_exp_f32_e32 v235, v130
	s_and_saveexec_b64 s[4:5], vcc
	ds_write_b32 v199, v235
	s_or_b64 exec, exec, s[4:5]
	s_waitcnt lgkmcnt(0)
	ds_read_b128 v[142:145], v214 offset:96
	ds_read_b128 v[138:141], v214 offset:64
	ds_read_b128 v[134:137], v214 offset:32
	ds_read_b128 v[130:133], v214
	s_waitcnt lgkmcnt(0)
	v_pk_mul_f32 v[16:17], v[16:17], v[144:145]
	v_pk_mul_f32 v[12:13], v[12:13], v[140:141]
	v_pk_mul_f32 v[8:9], v[8:9], v[136:137]
	v_pk_mul_f32 v[4:5], v[4:5], v[132:133]
	v_pk_mul_f32 v[14:15], v[14:15], v[142:143]
	v_pk_mul_f32 v[10:11], v[10:11], v[138:139]
	v_pk_mul_f32 v[6:7], v[6:7], v[134:135]
	v_pk_mul_f32 v[2:3], v[2:3], v[130:131]
	v_pk_mul_f32 v[128:129], v[128:129], v[144:145]
	v_pk_mul_f32 v[124:125], v[124:125], v[140:141]
	v_pk_mul_f32 v[120:121], v[120:121], v[136:137]
	v_pk_mul_f32 v[116:117], v[116:117], v[132:133]
	v_pk_mul_f32 v[126:127], v[126:127], v[142:143]
	v_pk_mul_f32 v[122:123], v[122:123], v[138:139]
	v_pk_mul_f32 v[118:119], v[118:119], v[134:135]
	v_pk_mul_f32 v[114:115], v[114:115], v[130:131]
	v_pk_mul_f32 v[112:113], v[112:113], v[144:145]
	v_pk_mul_f32 v[108:109], v[108:109], v[140:141]
	v_pk_mul_f32 v[104:105], v[104:105], v[136:137]
	v_pk_mul_f32 v[100:101], v[100:101], v[132:133]
	v_pk_mul_f32 v[110:111], v[110:111], v[142:143]
	v_pk_mul_f32 v[106:107], v[106:107], v[138:139]
	v_pk_mul_f32 v[102:103], v[102:103], v[134:135]
	v_pk_mul_f32 v[98:99], v[98:99], v[130:131]
	v_pk_mul_f32 v[96:97], v[96:97], v[144:145]
	v_pk_mul_f32 v[92:93], v[92:93], v[140:141]
	v_pk_mul_f32 v[88:89], v[88:89], v[136:137]
	v_pk_mul_f32 v[84:85], v[84:85], v[132:133]
	v_pk_mul_f32 v[94:95], v[94:95], v[142:143]
	v_pk_mul_f32 v[90:91], v[90:91], v[138:139]
	v_pk_mul_f32 v[86:87], v[86:87], v[134:135]
	v_pk_mul_f32 v[82:83], v[82:83], v[130:131]
	v_pk_mul_f32 v[80:81], v[80:81], v[144:145]
	v_pk_mul_f32 v[76:77], v[76:77], v[140:141]
	v_pk_mul_f32 v[72:73], v[72:73], v[136:137]
	v_pk_mul_f32 v[68:69], v[68:69], v[132:133]
	v_pk_mul_f32 v[78:79], v[78:79], v[142:143]
	v_pk_mul_f32 v[74:75], v[74:75], v[138:139]
	v_pk_mul_f32 v[70:71], v[70:71], v[134:135]
	v_pk_mul_f32 v[66:67], v[66:67], v[130:131]
	v_pk_mul_f32 v[64:65], v[64:65], v[144:145]
	v_pk_mul_f32 v[60:61], v[60:61], v[140:141]
	v_pk_mul_f32 v[56:57], v[56:57], v[136:137]
	v_pk_mul_f32 v[52:53], v[52:53], v[132:133]
	v_pk_mul_f32 v[62:63], v[62:63], v[142:143]
	v_pk_mul_f32 v[58:59], v[58:59], v[138:139]
	v_pk_mul_f32 v[54:55], v[54:55], v[134:135]
	v_pk_mul_f32 v[50:51], v[50:51], v[130:131]
	v_pk_mul_f32 v[48:49], v[48:49], v[144:145]
	v_pk_mul_f32 v[44:45], v[44:45], v[140:141]
	v_pk_mul_f32 v[40:41], v[40:41], v[136:137]
	v_pk_mul_f32 v[36:37], v[36:37], v[132:133]
	v_pk_mul_f32 v[46:47], v[46:47], v[142:143]
	v_pk_mul_f32 v[42:43], v[42:43], v[138:139]
	v_pk_mul_f32 v[38:39], v[38:39], v[134:135]
	v_pk_mul_f32 v[34:35], v[34:35], v[130:131]
	v_pk_mul_f32 v[32:33], v[32:33], v[144:145]
	v_pk_mul_f32 v[28:29], v[28:29], v[140:141]
	v_pk_mul_f32 v[24:25], v[24:25], v[136:137]
	v_pk_mul_f32 v[20:21], v[20:21], v[132:133]
	v_pk_mul_f32 v[30:31], v[30:31], v[142:143]
	v_pk_mul_f32 v[26:27], v[26:27], v[138:139]
	v_pk_mul_f32 v[22:23], v[22:23], v[134:135]
	v_pk_mul_f32 v[18:19], v[18:19], v[130:131]
	s_branch .LBB0_631
